# stack: relaxed unit-top waits in both MoE GEMMs + double-buffered P0 x->bf16 loop on top of previous
# speedup vs baseline: 1.0041x; 1.0001x over previous
;     __device__ __forceinline__ void init(f32x4 (&acc)[2][2][4][2], const Pre& p) const {
; #pragma unroll
;         for (int a = 0; a < 2; ++a)
; #pragma unroll
;             for (int m = 0; m < 4; ++m) { acc[a][0][m][0] = p.v[0]; acc[a][0][m][1] = p.v[1]; acc[a][1][m][0] = p.v[2]; acc[a][1][m][1] = p.v[3]; } }
; template <class Epi, class Sched, bool ALIGN_EPI = false, bool SP2 = false, bool GATHER = false>
; __device__ __forceinline__ void gemm_phase(PG8_LAS unsigned char* lds, const Gemm g, const Sched& S, const Epi& E, const int2* gslot = nullptr, PG8_LAS unsigned char* gtab = nullptr) {
;     ...
;         E.init(acc, pre);
;         cur = nxt; cA = nA; cB = nB; ++ui;
.LBB0_1080:
	s_waitcnt vmcnt(8)
	v_mov_b64_e32 v[10:11], v[138:139]
	v_mov_b64_e32 v[14:15], v[142:143]
	v_mov_b64_e32 v[18:19], v[138:139]
	v_mov_b64_e32 v[22:23], v[142:143]
	v_mov_b64_e32 v[2:3], v[130:131]
	v_mov_b64_e32 v[6:7], v[134:135]
	v_mov_b64_e32 v[26:27], v[130:131]
	v_mov_b64_e32 v[30:31], v[134:135]
	v_mov_b64_e32 v[34:35], v[130:131]
	v_mov_b64_e32 v[38:39], v[134:135]
	v_mov_b64_e32 v[42:43], v[130:131]
	v_mov_b64_e32 v[46:47], v[134:135]
	v_mov_b64_e32 v[50:51], v[138:139]
	v_mov_b64_e32 v[54:55], v[142:143]
	v_mov_b64_e32 v[58:59], v[138:139]
	v_mov_b64_e32 v[62:63], v[142:143]
	v_mov_b64_e32 v[66:67], v[138:139]
	v_mov_b64_e32 v[70:71], v[142:143]
	v_mov_b64_e32 v[74:75], v[138:139]
	v_mov_b64_e32 v[78:79], v[142:143]
	v_mov_b64_e32 v[82:83], v[130:131]
	v_mov_b64_e32 v[86:87], v[134:135]
	v_mov_b64_e32 v[90:91], v[130:131]
	v_mov_b64_e32 v[94:95], v[134:135]
	v_mov_b64_e32 v[98:99], v[130:131]
	v_mov_b64_e32 v[106:107], v[134:135]
	v_mov_b64_e32 v[114:115], v[130:131]
	v_mov_b64_e32 v[122:123], v[134:135]
	v_mov_b64_e32 v[102:103], v[142:143]
	v_mov_b64_e32 v[110:111], v[138:139]
	v_mov_b64_e32 v[118:119], v[142:143]
	v_mov_b64_e32 v[126:127], v[138:139]
	v_mov_b32_e32 v158, v160
	v_mov_b32_e32 v156, v187
	v_mov_b32_e32 v154, v186
	v_mov_b32_e32 v152, v185
	v_mov_b64_e32 v[12:13], v[140:141]
	v_mov_b64_e32 v[16:17], v[144:145]
	v_mov_b64_e32 v[20:21], v[140:141]
	v_mov_b64_e32 v[24:25], v[144:145]
	v_mov_b64_e32 v[4:5], v[132:133]
	v_mov_b64_e32 v[8:9], v[136:137]
	v_mov_b64_e32 v[28:29], v[132:133]
	v_mov_b64_e32 v[32:33], v[136:137]
	v_mov_b64_e32 v[36:37], v[132:133]
	v_mov_b64_e32 v[40:41], v[136:137]
	v_mov_b64_e32 v[44:45], v[132:133]
	v_mov_b64_e32 v[48:49], v[136:137]
	v_mov_b64_e32 v[52:53], v[140:141]
	v_mov_b64_e32 v[56:57], v[144:145]
	v_mov_b64_e32 v[60:61], v[140:141]
	v_mov_b64_e32 v[64:65], v[144:145]
	v_mov_b64_e32 v[68:69], v[140:141]
	v_mov_b64_e32 v[72:73], v[144:145]
	v_mov_b64_e32 v[76:77], v[140:141]
	v_mov_b64_e32 v[80:81], v[144:145]
	v_mov_b64_e32 v[84:85], v[132:133]
	v_mov_b64_e32 v[88:89], v[136:137]
	v_mov_b64_e32 v[92:93], v[132:133]
	v_mov_b64_e32 v[96:97], v[136:137]
	v_mov_b64_e32 v[100:101], v[132:133]
	v_mov_b64_e32 v[108:109], v[136:137]
	v_mov_b64_e32 v[116:117], v[132:133]
	v_mov_b64_e32 v[124:125], v[136:137]
	v_mov_b64_e32 v[104:105], v[144:145]
	v_mov_b64_e32 v[112:113], v[140:141]
	v_mov_b64_e32 v[120:121], v[144:145]
	v_mov_b64_e32 v[128:129], v[140:141]
	s_mov_b32 s62, s93
	s_mov_b32 s90, s74
	s_mov_b32 s58, s20
	s_mov_b32 s45, s91
	s_andn2_b64 vcc, exec, s[4:5]
	s_mov_b64 s[10:11], s[52:53]
	s_cbranch_vccz .LBB0_1103

; #define PG8_GDMA(u, par) do { int gl_ = lane; asm volatile("" : "+v"(gl_));        \
;         if (wid < 2) __builtin_amdgcn_global_load_lds((const unsigned*)((const char*)gslot + ((size_t)(u).aux * GCAP + (size_t)(u).lt * 256) * 8 + (size_t)(wid * 64 + gl_) * 16), \
;         (PG8_LAS unsigned*)(gtab + (par) * 2048 + wid * 1024), 16, 0, 0); } while (0)
; template <class Epi, class Sched, bool ALIGN_EPI = false, bool SP2 = false, bool GATHER = false>
; __device__ __forceinline__ void gemm_phase(PG8_LAS unsigned char* lds, const Gemm g, const Sched& S, const Epi& E, const int2* gslot = nullptr, PG8_LAS unsigned char* gtab = nullptr) {
;     ...
;         if constexpr (GATHER) { if (has_next) PG8_GDMA(nxt, (ui + 1) & 1); }
.LBB0_1087:
	v_cndmask_b32_e64 v0, 0, 1, s[8:9]
	v_cmp_ne_u32_e64 s[6:7], 1, v0
	s_andn2_b64 vcc, exec, s[8:9]
	s_mov_b64 s[52:53], s[10:11]
	s_cbranch_vccnz .LBB0_1091
	v_mov_b32_e32 v0, v168
	s_andn2_b64 vcc, exec, s[22:23]
	s_cbranch_vccnz .LBB0_1090
	s_ashr_i32 s21, s20, 31
	s_ashr_i32 s65, s64, 31
	s_lshl_b64 s[8:9], s[64:65], 11
	s_lshl_b64 s[12:13], s[20:21], 18
	s_add_u32 s12, s51, s12
	s_addc_u32 s13, s46, s13
	s_add_u32 s8, s12, s8
	v_add_u32_e32 v130, s44, v0
	s_addc_u32 s9, s13, s9
	v_ashrrev_i32_e32 v131, 31, v130
	v_lshl_add_u64 v[130:131], v[130:131], 4, s[8:9]
	s_lshl_b32 s8, s91, 11
	s_and_b32 s8, s8, 0x800
	s_add_i32 m0, s87, s8
	s_nop 0
	global_load_lds_dwordx4 v[130:131], off

;     __device__ __forceinline__ void init(f32x4 (&acc)[2][2][4][2], const Pre& p) const {
; #pragma unroll
;         for (int bj = 0; bj < 2; ++bj)
; #pragma unroll
;             for (int a = 0; a < 2; ++a)
; #pragma unroll
;                 for (int m = 0; m < 4; ++m) { acc[a][bj][m][0] = p.v[2 * bj]; acc[a][bj][m][1] = p.v[2 * bj + 1]; } }
; template <class Epi, class Sched, bool ALIGN_EPI = false, bool SP2 = false, bool GATHER = false>
; __device__ __forceinline__ void gemm_phase(PG8_LAS unsigned char* lds, const Gemm g, const Sched& S, const Epi& E, const int2* gslot = nullptr, PG8_LAS unsigned char* gtab = nullptr) {
;     ...
;         const char* nA = (has_next && !GATHER) ? (const char*)g.A + (size_t)nxt.pm * tstep : cA; const char* nB = has_next ? (const char*)g.Bt + (size_t)nxt.pb * tstep : cB;
.LBB0_1173:
	s_ashr_i32 s29, s28, 31
	s_lshl_b64 s[14:15], s[28:29], 19
	s_add_u32 s34, s0, s14
	s_addc_u32 s35, s38, s15
	s_and_b64 s[14:15], s[30:31], exec
	s_cselect_b32 s7, s35, s13
	s_cselect_b32 s9, s34, s12
	s_ashr_i32 s27, s26, 31
	s_lshl_b64 s[14:15], s[26:27], 19
	s_add_u32 s36, s39, s14
	s_addc_u32 s37, s42, s15
	s_and_b64 s[14:15], s[30:31], exec
	s_cselect_b32 s18, s37, s11
	s_cselect_b32 s19, s36, s10
	s_add_u32 s12, s12, 0x40080
	s_addc_u32 s13, s13, 0
	s_add_u32 s27, s10, 0x100
	s_waitcnt vmcnt(16)
	v_mov_b64_e32 v[20:21], v[4:5]
	v_mov_b64_e32 v[24:25], v[8:9]
	v_mov_b64_e32 v[36:37], v[4:5]
	v_mov_b64_e32 v[40:41], v[8:9]
	v_mov_b64_e32 v[52:53], v[4:5]
	v_mov_b64_e32 v[56:57], v[8:9]
	v_mov_b64_e32 v[28:29], v[12:13]
	v_mov_b64_e32 v[32:33], v[16:17]
	v_mov_b64_e32 v[44:45], v[12:13]
	v_mov_b64_e32 v[48:49], v[16:17]
	v_mov_b64_e32 v[60:61], v[12:13]
	v_mov_b64_e32 v[64:65], v[16:17]
	v_mov_b64_e32 v[84:85], v[4:5]
	v_mov_b64_e32 v[88:89], v[8:9]
	v_mov_b64_e32 v[100:101], v[4:5]
	v_mov_b64_e32 v[104:105], v[8:9]
	v_mov_b64_e32 v[116:117], v[4:5]
	v_mov_b64_e32 v[120:121], v[8:9]
	v_mov_b64_e32 v[132:133], v[4:5]
	v_mov_b64_e32 v[136:137], v[8:9]
	v_mov_b64_e32 v[92:93], v[12:13]
	v_mov_b64_e32 v[96:97], v[16:17]
	v_mov_b64_e32 v[108:109], v[12:13]
	v_mov_b64_e32 v[112:113], v[16:17]
	v_mov_b64_e32 v[124:125], v[12:13]
	v_mov_b64_e32 v[128:129], v[16:17]
	v_mov_b64_e32 v[140:141], v[12:13]
	v_mov_b64_e32 v[144:145], v[16:17]
	s_addc_u32 s29, s11, 0
	s_mov_b32 s67, -2
	v_mov_b64_e32 v[18:19], v[2:3]
	v_mov_b64_e32 v[22:23], v[6:7]
	v_mov_b64_e32 v[34:35], v[2:3]
	v_mov_b64_e32 v[38:39], v[6:7]
	v_mov_b64_e32 v[50:51], v[2:3]
	v_mov_b64_e32 v[54:55], v[6:7]
	v_mov_b64_e32 v[26:27], v[10:11]
	v_mov_b64_e32 v[30:31], v[14:15]
	v_mov_b64_e32 v[42:43], v[10:11]
	v_mov_b64_e32 v[46:47], v[14:15]
	v_mov_b64_e32 v[58:59], v[10:11]
	v_mov_b64_e32 v[62:63], v[14:15]
	v_mov_b64_e32 v[82:83], v[2:3]
	v_mov_b64_e32 v[86:87], v[6:7]
	v_mov_b64_e32 v[98:99], v[2:3]
	v_mov_b64_e32 v[102:103], v[6:7]
	v_mov_b64_e32 v[114:115], v[2:3]
	v_mov_b64_e32 v[118:119], v[6:7]
	v_mov_b64_e32 v[130:131], v[2:3]
	v_mov_b64_e32 v[134:135], v[6:7]
	v_mov_b64_e32 v[90:91], v[10:11]
	v_mov_b64_e32 v[94:95], v[14:15]
	v_mov_b64_e32 v[106:107], v[10:11]
	v_mov_b64_e32 v[110:111], v[14:15]
	v_mov_b64_e32 v[122:123], v[10:11]
	v_mov_b64_e32 v[126:127], v[14:15]
	v_mov_b64_e32 v[138:139], v[10:11]
	v_mov_b64_e32 v[142:143], v[14:15]
